# Layer-1 MoE gate/up weight conversion (half of the prologue's f32->bf16 queue) deferred: converted by workgroups that run out of NA work while GLA still runs, remainder drained at the end of the layer
# speedup vs baseline: 1.0099x; 1.0047x over previous
; #define LAS __attribute__((address_space(3)))
; __device__ __forceinline__ unsigned xb_add(unsigned* p, unsigned v) { return __hip_atomic_fetch_add(p, v, __ATOMIC_RELAXED, __HIP_MEMORY_SCOPE_AGENT); }
; __device__ __forceinline__ void phase_prologue(const Args& a, LAS unsigned char* lds) {
;     ...
;     unsigned* cq_head = (unsigned*)(a.ws + WS_CTL) + 8192 + 768;
;     volatile LAS int* qs = (volatile LAS int*)(lds + 128 * 129 * 4);
;     int pend = 0, it = 0;
;     if (tid == 0) { qs[0] = (int)xb_add(cq_head, 1u); pend = (int)xb_add(cq_head, 1u); }
;     __syncthreads();
;     for (int u = qs[0]; u < CTOT; u = qs[it & 1]) {
.LBB0_37:
	s_or_b64 exec, exec, s[6:7]
	s_add_i32 s6, 0, 0x10200
	v_mov_b32_e32 v2, s6
	s_waitcnt lgkmcnt(0)
	s_barrier
	ds_read_b32 v2, v2
	s_movk_i32 s6, 0x281f
	s_waitcnt lgkmcnt(0)
	v_cmp_lt_i32_e32 vcc, s6, v2
	v_readfirstlane_b32 s20, v2
	s_cbranch_vccnz .LBB0_79
	v_lshlrev_b32_e32 v2, 3, v0
	v_or_b32_e32 v6, 0xa00, v0
	v_and_b32_e32 v2, 0x78, v2
	s_movk_i32 s6, 0x204
	v_or_b32_e32 v4, 0x200, v0
	v_or_b32_e32 v5, 0x600, v0
	v_lshrrev_b32_e32 v40, 5, v6
	v_or_b32_e32 v6, 0xe00, v0
	v_or_b32_e32 v8, 0x400, v0
	v_mad_u32_u24 v3, v2, s6, 0
	v_lshrrev_b32_e32 v38, 5, v4
	v_lshrrev_b32_e32 v39, 5, v5
	v_lshrrev_b32_e32 v41, 5, v6
	v_lshrrev_b32_e32 v9, 5, v8
	v_lshrrev_b32_e32 v42, 4, v0
	v_lshrrev_b32_e32 v44, 4, v4
	v_lshrrev_b32_e32 v46, 4, v8
	v_lshrrev_b32_e32 v48, 4, v5
	v_mul_u32_u24_e32 v6, 0x204, v104
	v_mul_u32_u24_e32 v7, 0x204, v38
	v_mul_u32_u24_e32 v9, 0x204, v9
	v_mul_u32_u24_e32 v10, 0x204, v39
	v_mul_u32_u24_e32 v11, 0x204, v40
	v_lshl_add_u32 v43, v42, 2, v3
	v_lshl_add_u32 v45, v44, 2, v3
	v_lshl_add_u32 v47, v46, 2, v3
	v_lshl_add_u32 v49, v48, 2, v3
	v_mul_u32_u24_e32 v3, 0x204, v41
	v_mov_b32_e32 v35, 0
	v_or_b32_e32 v50, 32, v104
	v_or_b32_e32 v51, 64, v104
	v_or_b32_e32 v52, 0x60, v104
	s_mov_b32 s16, 1
	v_add_u32_e32 v53, v106, v6
	v_add_u32_e32 v54, v106, v7
	v_add_u32_e32 v55, v106, v9
	v_add_u32_e32 v56, v106, v10
	v_add_u32_e32 v57, v106, v11
	v_add_u32_e32 v58, v106, v3
	v_lshlrev_b32_e32 v34, 1, v2
	s_movk_i32 s17, 0x2820
	s_branch .LBB0_41

; __device__ __forceinline__ void phase_prologue(const Args& a, LAS unsigned char* lds) {
;     ...
;         int r = u; const float* src; int ldn, nvalid, NT, mode = 0; bf16_t* dst;
;         if (r < CJ0) { src = a.in[I_EVIN]; ldn = 6144; nvalid = 6144; NT = 48; dst = (bf16_t*)(a.ws + WS_WIN0); }
;         else if ((r -= CJ0) < CJ1) { src = a.in[I_EVOUT]; ldn = 2048; nvalid = 2048; NT = 16; dst = (bf16_t*)(a.ws + WS_WOUT0); }
;         else if ((r -= CJ1) < CJ2) { src = a.in[I_ODIN]; ldn = 6176; nvalid = 6176; NT = 50; dst = (bf16_t*)(a.ws + WS_WIN1); }
;         else if ((r -= CJ2) < CJ3) { src = a.in[I_ODOUT]; ldn = 2048; nvalid = 2048; NT = 16; dst = (bf16_t*)(a.ws + WS_WOUT1); }
;         else { r -= CJ3; const int which = r / CJM; r -= which * CJM; const int mtx = r >> 8; r &= 255; ldn = 2048; nvalid = 2048; NT = 16;
;             if (which == 0) { src = a.in[I_WGATE] + (size_t)mtx * 2048 * 2048; dst = (bf16_t*)(a.ws + WS_WGU) + (size_t)mtx * 4096 * 2048; mode = 1; }
;             else if (which == 1) { src = a.in[I_WUP] + (size_t)mtx * 2048 * 2048; dst = (bf16_t*)(a.ws + WS_WGU) + (size_t)mtx * 4096 * 2048; mode = 2; }
;             else { src = a.in[I_WDOWN] + (size_t)mtx * 2048 * 2048; dst = (bf16_t*)(a.ws + WS_WDN) + (size_t)mtx * 2048 * 2048; } }
;         const int kt = r / NT, ntl = r % NT, k0 = kt * 128, n0 = ntl * 128;
.LBB0_41:
	s_cmpk_lt_i32 s20, 0x300
	s_cbranch_scc1 .LBB0_50
	s_cmpk_gt_u32 s20, 0x3ff
	s_cbranch_scc0 .LBB0_51
	s_cmpk_gt_u32 s20, 0x71f
	s_cbranch_scc0 .LBB0_52
	s_cmpk_gt_u32 s20, 0x81f
	s_cbranch_scc0 .LBB0_53
	s_add_i32 s12, s20, 0xfffff7e0
	s_cmpk_gt_u32 s12, 0xfff
	s_cselect_b32 s6, 0x1000, 0
	s_add_i32 s12, s12, s6
	s_lshl_b32 s6, s12, 16
	s_and_b32 s13, s6, 0x1f000000
	v_readlane_b32 s6, v254, 25
	s_add_u32 s6, s6, s13
	v_readlane_b32 s7, v254, 26
	s_addc_u32 s7, s7, 0
	s_cmpk_gt_u32 s12, 0x1fff
	s_mov_b64 s[8:9], -1
	s_cbranch_scc0 .LBB0_47
	s_add_u32 s14, s88, s13
	s_addc_u32 s15, s89, 0
	s_mov_b64 s[8:9], 0

; __device__ __forceinline__ void gla_fast_unit(int unit, const bf16_t* P, const float* w_up, const float* b_up, float* Of, float* Ob, LAS unsigned char* lds0) {
;     ...
;     __syncthreads();
; __global__ void __launch_bounds__(512, 2) mk_fwd(Args a) {
;     ...
;         if (bid < 64) { gla_fast_unit(bid, Pb, a.in[I_GLAWUP], a.in[I_GLABUP], Of, Ob, lds); }
.LBB0_1205:
	s_waitcnt lgkmcnt(0)
	s_barrier
	v_cmp_eq_u32_e32 vcc, 0, v0
	s_and_saveexec_b64 s[6:7], vcc
	v_mov_b32_e32 v2, 0x9100
	v_mov_b32_e32 v3, 1
	global_atomic_add v2, v3, s[94:95]
	s_mov_b64 exec, s[6:7]

; __device__ __forceinline__ void phase_prologue(const Args& a, LAS unsigned char* lds) {
;     ...
;     for (int u = qs[0]; u < CTOT; u = qs[it & 1]) {
;         int r = u; const float* src; int ldn, nvalid, NT, mode = 0; bf16_t* dst;
;         if (r < CJ0) { src = a.in[I_EVIN]; ldn = 6144; nvalid = 6144; NT = 48; dst = (bf16_t*)(a.ws + WS_WIN0); }
;         else if ((r -= CJ0) < CJ1) { src = a.in[I_EVOUT]; ldn = 2048; nvalid = 2048; NT = 16; dst = (bf16_t*)(a.ws + WS_WOUT0); }
;         else if ((r -= CJ1) < CJ2) { src = a.in[I_ODIN]; ldn = 6176; nvalid = 6176; NT = 50; dst = (bf16_t*)(a.ws + WS_WIN1); }
;         else if ((r -= CJ2) < CJ3) { src = a.in[I_ODOUT]; ldn = 2048; nvalid = 2048; NT = 16; dst = (bf16_t*)(a.ws + WS_WOUT1); }
;         else { r -= CJ3; const int which = r / CJM; r -= which * CJM; const int mtx = r >> 8; r &= 255; ldn = 2048; nvalid = 2048; NT = 16;
;             if (which == 0) { src = a.in[I_WGATE] + (size_t)mtx * 2048 * 2048; dst = (bf16_t*)(a.ws + WS_WGU) + (size_t)mtx * 4096 * 2048; mode = 1; }
;             else if (which == 1) { src = a.in[I_WUP] + (size_t)mtx * 2048 * 2048; dst = (bf16_t*)(a.ws + WS_WGU) + (size_t)mtx * 4096 * 2048; mode = 2; }
;             else { src = a.in[I_WDOWN] + (size_t)mtx * 2048 * 2048; dst = (bf16_t*)(a.ws + WS_WDN) + (size_t)mtx * 2048 * 2048; } }
;         const int kt = r / NT, ntl = r % NT, k0 = kt * 128, n0 = ntl * 128;
.Lcva_entry:
	s_waitcnt vmcnt(0) lgkmcnt(0)
	s_barrier
	v_lshrrev_b32_e32 v104, 5, v0
	v_and_b32_e32 v126, 31, v0
	v_lshlrev_b32_e32 v105, 13, v104
	v_lshl_add_u32 v105, v126, 4, v105
	v_add_u32_e32 v106, 0x20000, v105
	v_add_u32_e32 v107, 0x40000, v105
	v_add_u32_e32 v108, 0x60000, v105
	v_add_u32_e32 v109, 0x80000, v105
	v_add_u32_e32 v110, 0xa0000, v105
	v_add_u32_e32 v111, 0xc0000, v105
	v_add_u32_e32 v112, 0xe0000, v105
	v_mul_u32_u24_e32 v113, 0x204, v104
	v_lshl_add_u32 v113, v126, 4, v113
	v_lshrrev_b32_e32 v127, 4, v0
	v_and_b32_e32 v126, 15, v0
	v_mul_u32_u24_e32 v114, 0x1020, v126
	v_lshl_add_u32 v114, v127, 2, v114
	v_lshlrev_b32_e32 v115, 12, v127
	v_lshl_add_u32 v115, v126, 4, v115
	v_add_u32_e32 v116, 0x20000, v115
	v_add_u32_e32 v117, 0x40000, v115
	v_add_u32_e32 v118, 0x60000, v115
	v_mov_b32_e32 v119, 1
	v_mov_b32_e32 v120, 0x9000
	v_mov_b32_e32 v121, 0x9100
	v_mov_b32_e32 v122, 0
	v_mov_b32_e32 v125, 0x10200
	s_mov_b32 s25, 0
	v_readlane_b32 s42, v254, 27
	v_readlane_b32 s43, v254, 28
	s_sub_u32 s42, s42, 0x28
	s_subb_u32 s43, s43, 0
	s_load_dwordx2 s[40:41], s[42:43], 0x0
	s_waitcnt lgkmcnt(0)
	v_cmp_eq_u32_e32 vcc, 0, v0
	s_and_saveexec_b64 s[34:35], vcc
	s_cbranch_execz .Lcva_f0
	global_atomic_add v124, v121, v122, s[94:95] sc0
	s_waitcnt vmcnt(0)
	ds_write_b32 v125, v124 offset:4
.Lcva_f0:
	s_mov_b64 exec, s[34:35]
	s_waitcnt lgkmcnt(0)
	s_barrier
	ds_read_b32 v127, v125 offset:4
	s_waitcnt lgkmcnt(0)
	v_readfirstlane_b32 s25, v127
	s_cmp_lg_u32 s25, 0
	s_cbranch_scc1 .Lcva_done
	s_barrier
	v_cmp_eq_u32_e32 vcc, 0, v0
	s_and_saveexec_b64 s[34:35], vcc
	s_cbranch_execz .Lcva_t0a
	global_atomic_add v123, v120, v119, s[94:95] sc0
	s_waitcnt vmcnt(0)
	ds_write_b32 v125, v123
	ds_write_b32 v125, v122 offset:4
.Lcva_t0a:
	s_mov_b64 exec, s[34:35]
	s_waitcnt lgkmcnt(0)
	s_barrier
.Lcva_loop:
	ds_read_b32 v126, v125
	ds_read_b32 v127, v125 offset:4
	s_waitcnt lgkmcnt(0)
	v_readfirstlane_b32 s24, v126
	v_readfirstlane_b32 s25, v127
	s_cmpk_gt_u32 s24, 0x1fff
	s_cbranch_scc1 .Lcva_done
	s_cmp_lg_u32 s25, 0
	s_cbranch_scc1 .Lcva_nopf
	v_cmp_eq_u32_e32 vcc, 0, v0
	s_and_saveexec_b64 s[34:35], vcc
	s_cbranch_execz .Lcva_t0b
	global_atomic_add v123, v120, v119, s[94:95] sc0
	global_atomic_add v124, v121, v122, s[94:95] sc0
.Lcva_t0b:
	s_mov_b64 exec, s[34:35]
; #define LAS __attribute__((address_space(3)))
; __device__ __forceinline__ void lds_barrier() { asm volatile("s_waitcnt lgkmcnt(0)" ::: "memory"); __builtin_amdgcn_s_barrier(); asm volatile("" ::: "memory"); }
; __device__ __forceinline__ unsigned xb_add(unsigned* p, unsigned v) { return __hip_atomic_fetch_add(p, v, __ATOMIC_RELAXED, __HIP_MEMORY_SCOPE_AGENT); }
; __device__ __forceinline__ void xcd_barrier(const XcdBarrier& b) {
;     asm volatile("s_waitcnt vmcnt(0)" ::: "memory");
;     __syncthreads();
;     if (threadIdx.x == 0) {
;         unsigned* bar = b.bar;
;         __builtin_amdgcn_s_waitcnt(0);
;         unsigned nloc = b.st[0], nx = b.st[1];
;         if (nloc == 0u) { xcd_barrier_complete(bar, b.x, nloc, nx); b.st[0] = nloc; b.st[1] = nx; }
;         const unsigned old = xb_add(&bar[XB_XSUB(b.x)], 1u);
; __device__ __forceinline__ void phase_prologue(const Args& a, LAS unsigned char* lds) {
;     ...
;         for (int i = 0; i < 8; ++i) { const int id = tid + 512 * i, row = id >> 5, c4 = id & 31, n = n0 + c4 * 4;
;             v[i] = (f32x4){0.f, 0.f, 0.f, 0.f};
;             if (n < nvalid) v[i] = *(const f32x4*)(src + (size_t)(k0 + row) * ldn + n); }
; #pragma unroll
;         for (int i = 0; i < 8; ++i) { const int id = tid + 512 * i, row = id >> 5, c4 = id & 31;
;             LAS float* tp = tile + row * 129 + c4 * 4; tp[0] = v[i][0]; tp[1] = v[i][1]; tp[2] = v[i][2]; tp[3] = v[i][3]; }
;         lds_barrier();
; #pragma unroll
;         for (int i = 0; i < 4; ++i) { const int piece = tid + 512 * i, nl = piece >> 4, kg = piece & 15; const LAS float* s = tile + (kg * 8) * 129 + nl;
;             u32x4 o; o.x = pk2(s[0], s[129]); o.y = pk2(s[258], s[387]); o.z = pk2(s[516], s[645]); o.w = pk2(s[774], s[903]);
;             *(u32x4*)(dst + (size_t)(drow0 + nl) * 2048 + k0 + kg * 8) = o; }
.Lcva_nopf:
	s_lshr_b32 s36, s24, 12
	s_bfe_u32 s30, s24, 0x40008
	s_add_i32 s30, s30, 16
	s_lshl_b32 s30, s30, 24
	s_bfe_u32 s31, s24, 0x40004
	s_and_b32 s32, s24, 15
	v_readlane_b32 s26, v254, 43
	v_readlane_b32 s27, v254, 44
	s_cmp_lg_u32 s36, 0
	s_cselect_b32 s26, s40, s26
	s_cselect_b32 s27, s41, s27
	s_lshl_b32 s33, s31, 20
	s_add_i32 s33, s33, s30
	s_lshl_b32 s37, s32, 9
	s_add_i32 s33, s33, s37
	s_add_u32 s26, s26, s33
	s_addc_u32 s27, s27, 0
	v_readlane_b32 s28, v254, 25
	v_readlane_b32 s29, v254, 26
	s_lshl_b32 s33, s32, 20
	s_add_i32 s33, s33, s30
	s_lshl_b32 s37, s36, 19
	s_add_i32 s33, s33, s37
	s_lshl_b32 s37, s31, 8
	s_add_i32 s33, s33, s37
	s_add_u32 s28, s28, s33
	s_addc_u32 s29, s29, 0
	global_load_dwordx4 v[128:131], v105, s[26:27]
	global_load_dwordx4 v[132:135], v106, s[26:27]
	global_load_dwordx4 v[136:139], v107, s[26:27]
	global_load_dwordx4 v[140:143], v108, s[26:27]
	global_load_dwordx4 v[144:147], v109, s[26:27]
	global_load_dwordx4 v[148:151], v110, s[26:27]
	global_load_dwordx4 v[152:155], v111, s[26:27]
	global_load_dwordx4 v[156:159], v112, s[26:27]
	s_waitcnt vmcnt(7)
	ds_write_b32 v113, v128
	ds_write_b32 v113, v129 offset:4
	ds_write_b32 v113, v130 offset:8
	ds_write_b32 v113, v131 offset:12
	s_waitcnt vmcnt(6)
	ds_write_b32 v113, v132 offset:8256
	ds_write_b32 v113, v133 offset:8260
	ds_write_b32 v113, v134 offset:8264
	ds_write_b32 v113, v135 offset:8268
	s_waitcnt vmcnt(5)
	ds_write_b32 v113, v136 offset:16512
	ds_write_b32 v113, v137 offset:16516
	ds_write_b32 v113, v138 offset:16520
	ds_write_b32 v113, v139 offset:16524
	s_waitcnt vmcnt(4)
	ds_write_b32 v113, v140 offset:24768
	ds_write_b32 v113, v141 offset:24772
	ds_write_b32 v113, v142 offset:24776
	ds_write_b32 v113, v143 offset:24780
	s_waitcnt vmcnt(3)
	ds_write_b32 v113, v144 offset:33024
	ds_write_b32 v113, v145 offset:33028
	ds_write_b32 v113, v146 offset:33032
	ds_write_b32 v113, v147 offset:33036
	s_waitcnt vmcnt(2)
	ds_write_b32 v113, v148 offset:41280
	ds_write_b32 v113, v149 offset:41284
	ds_write_b32 v113, v150 offset:41288
	ds_write_b32 v113, v151 offset:41292
	s_waitcnt vmcnt(1)
	ds_write_b32 v113, v152 offset:49536
	ds_write_b32 v113, v153 offset:49540
	ds_write_b32 v113, v154 offset:49544
	ds_write_b32 v113, v155 offset:49548
	s_waitcnt vmcnt(0)
	ds_write_b32 v113, v156 offset:57792
	ds_write_b32 v113, v157 offset:57796
	ds_write_b32 v113, v158 offset:57800
	ds_write_b32 v113, v159 offset:57804
	s_waitcnt lgkmcnt(0)
	s_barrier
	ds_read_b32 v160, v114
	ds_read_b32 v161, v114 offset:516
	ds_read_b32 v162, v114 offset:1032
	ds_read_b32 v163, v114 offset:1548
	ds_read_b32 v164, v114 offset:2064
	ds_read_b32 v165, v114 offset:2580
	ds_read_b32 v166, v114 offset:3096
	ds_read_b32 v167, v114 offset:3612
	s_waitcnt lgkmcnt(0)
	v_cvt_pk_bf16_f32 v168, v160, v161
	v_cvt_pk_bf16_f32 v169, v162, v163
	v_cvt_pk_bf16_f32 v170, v164, v165
	v_cvt_pk_bf16_f32 v171, v166, v167
	global_store_dwordx4 v115, v[168:171], s[28:29]
	ds_read_b32 v160, v114 offset:128
	ds_read_b32 v161, v114 offset:644
	ds_read_b32 v162, v114 offset:1160
	ds_read_b32 v163, v114 offset:1676
	ds_read_b32 v164, v114 offset:2192
	ds_read_b32 v165, v114 offset:2708
	ds_read_b32 v166, v114 offset:3224
	ds_read_b32 v167, v114 offset:3740
	s_waitcnt lgkmcnt(0)
	v_cvt_pk_bf16_f32 v172, v160, v161
	v_cvt_pk_bf16_f32 v173, v162, v163
	v_cvt_pk_bf16_f32 v174, v164, v165
	v_cvt_pk_bf16_f32 v175, v166, v167
	global_store_dwordx4 v116, v[172:175], s[28:29]
	ds_read_b32 v160, v114 offset:256
	ds_read_b32 v161, v114 offset:772
	ds_read_b32 v162, v114 offset:1288
	ds_read_b32 v163, v114 offset:1804
	ds_read_b32 v164, v114 offset:2320
	ds_read_b32 v165, v114 offset:2836
	ds_read_b32 v166, v114 offset:3352
	ds_read_b32 v167, v114 offset:3868
	s_waitcnt lgkmcnt(0)
	v_cvt_pk_bf16_f32 v168, v160, v161
	v_cvt_pk_bf16_f32 v169, v162, v163
	v_cvt_pk_bf16_f32 v170, v164, v165
	v_cvt_pk_bf16_f32 v171, v166, v167
	global_store_dwordx4 v117, v[168:171], s[28:29]
	ds_read_b32 v160, v114 offset:384
	ds_read_b32 v161, v114 offset:900
	ds_read_b32 v162, v114 offset:1416
	ds_read_b32 v163, v114 offset:1932
	ds_read_b32 v164, v114 offset:2448
	ds_read_b32 v165, v114 offset:2964
	ds_read_b32 v166, v114 offset:3480
	ds_read_b32 v167, v114 offset:3996
	s_waitcnt lgkmcnt(0)
	v_cvt_pk_bf16_f32 v172, v160, v161
	v_cvt_pk_bf16_f32 v173, v162, v163
	v_cvt_pk_bf16_f32 v174, v164, v165
	v_cvt_pk_bf16_f32 v175, v166, v167
	global_store_dwordx4 v118, v[172:175], s[28:29]
	s_cmp_lg_u32 s25, 0
	s_cbranch_scc1 .Lcva_done
	v_cmp_eq_u32_e32 vcc, 0, v0
	s_and_saveexec_b64 s[34:35], vcc
	s_cbranch_execz .Lcva_t0c
	s_waitcnt vmcnt(0)
	ds_write_b32 v125, v123
	ds_write_b32 v125, v124 offset:4
.Lcva_t0c:
	s_mov_b64 exec, s[34:35]
	s_waitcnt lgkmcnt(0)
	s_barrier
	s_branch .Lcva_loop
.Lcva_done:
	s_branch .LBB0_1316
.LBB0_1316:
	v_readlane_b32 s0, v254, 0
	v_readlane_b32 s1, v254, 1
	s_cmp_gt_i32 s1, 14
	s_cselect_b64 s[0:1], -1, 0
	s_and_b64 s[2:3], s[22:23], s[0:1]
	s_andn2_b64 vcc, exec, s[2:3]
	s_cbranch_vccnz .LBB0_1366
	s_waitcnt vmcnt(0)
	v_cmp_eq_u32_e32 vcc, 0, v0
	s_waitcnt vmcnt(0) lgkmcnt(0)
	s_barrier
	s_and_saveexec_b64 s[2:3], vcc
	s_cbranch_execz .LBB0_1365
	s_add_i32 s4, 0, 0x23fc0
	v_mov_b32_e32 v1, s4
	s_waitcnt vmcnt(0) expcnt(0) lgkmcnt(0)
	ds_read_b32 v3, v1
	s_add_i32 s4, 0, 0x23fc4
	v_mov_b32_e32 v1, s4
	ds_read_b32 v1, v1
	s_waitcnt lgkmcnt(1)
	v_cmp_ne_u32_e32 vcc, 0, v3
	s_cbranch_vccnz .LBB0_1333
	v_readlane_b32 s4, v254, 27
	v_readlane_b32 s5, v254, 28
	s_load_dwordx2 s[8:9], s[4:5], 0x4
	s_add_u32 s4, s94, 0x4200
	s_addc_u32 s5, s95, 0
	s_add_u32 s6, s94, 0x4400
	s_addc_u32 s7, s95, 0
	v_readlane_b32 s10, v255, 9
	s_waitcnt lgkmcnt(0)
	s_mul_i32 s33, s8, s10
	s_add_u32 s8, s94, 0x4500
	s_mul_i32 s33, s33, s9
	s_addc_u32 s9, s95, 0
	s_add_u32 s10, s94, 0x4600
	s_addc_u32 s11, s95, 0
	s_add_u32 s12, s94, 0x4700
	s_addc_u32 s13, s95, 0
	s_add_u32 s14, s94, 0x4800
	s_addc_u32 s15, s95, 0
	s_add_u32 s16, s94, 0x4900
	s_addc_u32 s17, s95, 0
	s_add_u32 s18, s94, 0x4a00
	s_addc_u32 s19, s95, 0
	s_add_u32 s20, s94, 0x4b00
	s_addc_u32 s21, s95, 0
	s_add_u32 s22, s94, 0x4c00
	s_addc_u32 s23, s95, 0
	s_add_u32 s24, s94, 0x4d00
	s_addc_u32 s25, s95, 0
	s_add_u32 s26, s94, 0x4e00
	s_addc_u32 s27, s95, 0
	s_add_u32 s28, s94, 0x4f00
	s_addc_u32 s29, s95, 0
	s_add_u32 s30, s94, 0x5000
	s_addc_u32 s31, s95, 0
	s_add_u32 s34, s94, 0x5100
	s_addc_u32 s35, s95, 0
	s_add_u32 s36, s94, 0x5200
	s_addc_u32 s37, s95, 0
	s_add_u32 s38, s94, 0x5300
	s_addc_u32 s39, s95, 0
	s_mov_b32 s46, 1
	v_mov_b32_e32 v17, 0
	s_branch .LBB0_1321

; #define LAS __attribute__((address_space(3)))
; __device__ __forceinline__ unsigned xb_add(unsigned* p, unsigned v) { return __hip_atomic_fetch_add(p, v, __ATOMIC_RELAXED, __HIP_MEMORY_SCOPE_AGENT); }
; __device__ __forceinline__ void phase_prologue(const Args& a, LAS unsigned char* lds) {
;     ...
;     unsigned* cq_head = (unsigned*)(a.ws + WS_CTL) + 8192 + 768;
;     volatile LAS int* qs = (volatile LAS int*)(lds + 128 * 129 * 4);
;     int pend = 0, it = 0;
;     if (tid == 0) { qs[0] = (int)xb_add(cq_head, 1u); pend = (int)xb_add(cq_head, 1u); }
;     __syncthreads();
;     for (int u = qs[0]; u < CTOT; u = qs[it & 1]) {
;         int r = u; const float* src; int ldn, nvalid, NT, mode = 0; bf16_t* dst;
;         if (r < CJ0) { src = a.in[I_EVIN]; ldn = 6144; nvalid = 6144; NT = 48; dst = (bf16_t*)(a.ws + WS_WIN0); }
;         else if ((r -= CJ0) < CJ1) { src = a.in[I_EVOUT]; ldn = 2048; nvalid = 2048; NT = 16; dst = (bf16_t*)(a.ws + WS_WOUT0); }
;         else if ((r -= CJ1) < CJ2) { src = a.in[I_ODIN]; ldn = 6176; nvalid = 6176; NT = 50; dst = (bf16_t*)(a.ws + WS_WIN1); }
;         else if ((r -= CJ2) < CJ3) { src = a.in[I_ODOUT]; ldn = 2048; nvalid = 2048; NT = 16; dst = (bf16_t*)(a.ws + WS_WOUT1); }
;         else { r -= CJ3; const int which = r / CJM; r -= which * CJM; const int mtx = r >> 8; r &= 255; ldn = 2048; nvalid = 2048; NT = 16;
;             if (which == 0) { src = a.in[I_WGATE] + (size_t)mtx * 2048 * 2048; dst = (bf16_t*)(a.ws + WS_WGU) + (size_t)mtx * 4096 * 2048; mode = 1; }
;             else if (which == 1) { src = a.in[I_WUP] + (size_t)mtx * 2048 * 2048; dst = (bf16_t*)(a.ws + WS_WGU) + (size_t)mtx * 4096 * 2048; mode = 2; }
;             else { src = a.in[I_WDOWN] + (size_t)mtx * 2048 * 2048; dst = (bf16_t*)(a.ws + WS_WDN) + (size_t)mtx * 2048 * 2048; } }
;         const int kt = r / NT, ntl = r % NT, k0 = kt * 128, n0 = ntl * 128;
.LBB0_1442:
.Lcvb_entry:
	s_waitcnt vmcnt(0) lgkmcnt(0)
	s_barrier
	v_lshrrev_b32_e32 v104, 5, v0
	v_and_b32_e32 v126, 31, v0
	v_lshlrev_b32_e32 v105, 13, v104
	v_lshl_add_u32 v105, v126, 4, v105
	v_add_u32_e32 v106, 0x20000, v105
	v_add_u32_e32 v107, 0x40000, v105
	v_add_u32_e32 v108, 0x60000, v105
	v_add_u32_e32 v109, 0x80000, v105
	v_add_u32_e32 v110, 0xa0000, v105
	v_add_u32_e32 v111, 0xc0000, v105
	v_add_u32_e32 v112, 0xe0000, v105
	v_mul_u32_u24_e32 v113, 0x204, v104
	v_lshl_add_u32 v113, v126, 4, v113
	v_lshrrev_b32_e32 v127, 4, v0
	v_and_b32_e32 v126, 15, v0
	v_mul_u32_u24_e32 v114, 0x1020, v126
	v_lshl_add_u32 v114, v127, 2, v114
	v_lshlrev_b32_e32 v115, 12, v127
	v_lshl_add_u32 v115, v126, 4, v115
	v_add_u32_e32 v116, 0x20000, v115
	v_add_u32_e32 v117, 0x40000, v115
	v_add_u32_e32 v118, 0x60000, v115
	v_mov_b32_e32 v119, 1
	v_mov_b32_e32 v120, 0x9000
	v_mov_b32_e32 v121, 0x9100
	v_mov_b32_e32 v122, 0
	v_mov_b32_e32 v125, 0x10200
	s_mov_b32 s25, 0
	v_readlane_b32 s42, v254, 27
	v_readlane_b32 s43, v254, 28
	s_sub_u32 s42, s42, 0x28
	s_subb_u32 s43, s43, 0
	s_load_dwordx2 s[40:41], s[42:43], 0x0
	s_waitcnt lgkmcnt(0)
	v_cmp_eq_u32_e32 vcc, 0, v0
	s_and_saveexec_b64 s[34:35], vcc
	s_cbranch_execz .Lcvb_t0a
	global_atomic_add v123, v120, v119, s[94:95] sc0
	s_waitcnt vmcnt(0)
	ds_write_b32 v125, v123

; __device__ __forceinline__ void phase_prologue(const Args& a, LAS unsigned char* lds) {
;     ...
;         int r = u; const float* src; int ldn, nvalid, NT, mode = 0; bf16_t* dst;
;         if (r < CJ0) { src = a.in[I_EVIN]; ldn = 6144; nvalid = 6144; NT = 48; dst = (bf16_t*)(a.ws + WS_WIN0); }
;         else if ((r -= CJ0) < CJ1) { src = a.in[I_EVOUT]; ldn = 2048; nvalid = 2048; NT = 16; dst = (bf16_t*)(a.ws + WS_WOUT0); }
;         else if ((r -= CJ1) < CJ2) { src = a.in[I_ODIN]; ldn = 6176; nvalid = 6176; NT = 50; dst = (bf16_t*)(a.ws + WS_WIN1); }
;         else if ((r -= CJ2) < CJ3) { src = a.in[I_ODOUT]; ldn = 2048; nvalid = 2048; NT = 16; dst = (bf16_t*)(a.ws + WS_WOUT1); }
;         else { r -= CJ3; const int which = r / CJM; r -= which * CJM; const int mtx = r >> 8; r &= 255; ldn = 2048; nvalid = 2048; NT = 16;
;             if (which == 0) { src = a.in[I_WGATE] + (size_t)mtx * 2048 * 2048; dst = (bf16_t*)(a.ws + WS_WGU) + (size_t)mtx * 4096 * 2048; mode = 1; }
;             else if (which == 1) { src = a.in[I_WUP] + (size_t)mtx * 2048 * 2048; dst = (bf16_t*)(a.ws + WS_WGU) + (size_t)mtx * 4096 * 2048; mode = 2; }
;             else { src = a.in[I_WDOWN] + (size_t)mtx * 2048 * 2048; dst = (bf16_t*)(a.ws + WS_WDN) + (size_t)mtx * 2048 * 2048; } }
;         const int kt = r / NT, ntl = r % NT, k0 = kt * 128, n0 = ntl * 128;
;         const int drow0 = mode == 0 ? n0 : (ntl * 256 + (mode == 2 ? 128 : 0));
;         f32x4 v[8];
; #pragma unroll
;         for (int i = 0; i < 8; ++i) { const int id = tid + 512 * i, row = id >> 5, c4 = id & 31, n = n0 + c4 * 4;
;             v[i] = (f32x4){0.f, 0.f, 0.f, 0.f};
;             if (n < nvalid) v[i] = *(const f32x4*)(src + (size_t)(k0 + row) * ldn + n); }
; #pragma unroll
;         for (int i = 0; i < 8; ++i) { const int id = tid + 512 * i, row = id >> 5, c4 = id & 31;
;             LAS float* tp = tile + row * 129 + c4 * 4; tp[0] = v[i][0]; tp[1] = v[i][1]; tp[2] = v[i][2]; tp[3] = v[i][3]; }
;         lds_barrier();
; #pragma unroll
;         for (int i = 0; i < 4; ++i) { const int piece = tid + 512 * i, nl = piece >> 4, kg = piece & 15; const LAS float* s = tile + (kg * 8) * 129 + nl;
;             u32x4 o; o.x = pk2(s[0], s[129]); o.y = pk2(s[258], s[387]); o.z = pk2(s[516], s[645]); o.w = pk2(s[774], s[903]);
;             *(u32x4*)(dst + (size_t)(drow0 + nl) * 2048 + k0 + kg * 8) = o; }
;         ++it;
.Lcvb_loop:
	ds_read_b32 v126, v125
	s_waitcnt lgkmcnt(0)
	v_readfirstlane_b32 s24, v126
	s_cmpk_gt_u32 s24, 0x1fff
	s_cbranch_scc1 .Lcvb_done
	v_cmp_eq_u32_e32 vcc, 0, v0
	s_and_saveexec_b64 s[34:35], vcc
	s_cbranch_execz .Lcvb_t0b
	global_atomic_add v123, v120, v119, s[94:95] sc0
.Lcvb_t0b:
	s_mov_b64 exec, s[34:35]
	s_lshr_b32 s36, s24, 12
	s_bfe_u32 s30, s24, 0x40008
	s_add_i32 s30, s30, 16
	s_lshl_b32 s30, s30, 24
	s_bfe_u32 s31, s24, 0x40004
	s_and_b32 s32, s24, 15
	v_readlane_b32 s26, v254, 43
	v_readlane_b32 s27, v254, 44
	s_cmp_lg_u32 s36, 0
	s_cselect_b32 s26, s40, s26
	s_cselect_b32 s27, s41, s27
	s_lshl_b32 s33, s31, 20
	s_add_i32 s33, s33, s30
	s_lshl_b32 s37, s32, 9
	s_add_i32 s33, s33, s37
	s_add_u32 s26, s26, s33
	s_addc_u32 s27, s27, 0
	v_readlane_b32 s28, v254, 25
	v_readlane_b32 s29, v254, 26
	s_lshl_b32 s33, s32, 20
	s_add_i32 s33, s33, s30
	s_lshl_b32 s37, s36, 19
	s_add_i32 s33, s33, s37
	s_lshl_b32 s37, s31, 8
	s_add_i32 s33, s33, s37
	s_add_u32 s28, s28, s33
	s_addc_u32 s29, s29, 0
	global_load_dwordx4 v[128:131], v105, s[26:27]
	global_load_dwordx4 v[132:135], v106, s[26:27]
	global_load_dwordx4 v[136:139], v107, s[26:27]
	global_load_dwordx4 v[140:143], v108, s[26:27]
	global_load_dwordx4 v[144:147], v109, s[26:27]
	global_load_dwordx4 v[148:151], v110, s[26:27]
	global_load_dwordx4 v[152:155], v111, s[26:27]
	global_load_dwordx4 v[156:159], v112, s[26:27]
	s_waitcnt vmcnt(7)
	ds_write_b32 v113, v128
	ds_write_b32 v113, v129 offset:4
	ds_write_b32 v113, v130 offset:8
	ds_write_b32 v113, v131 offset:12
	s_waitcnt vmcnt(6)
	ds_write_b32 v113, v132 offset:8256
	ds_write_b32 v113, v133 offset:8260
	ds_write_b32 v113, v134 offset:8264
	ds_write_b32 v113, v135 offset:8268
	s_waitcnt vmcnt(5)
	ds_write_b32 v113, v136 offset:16512
	ds_write_b32 v113, v137 offset:16516
	ds_write_b32 v113, v138 offset:16520
	ds_write_b32 v113, v139 offset:16524
	s_waitcnt vmcnt(4)
	ds_write_b32 v113, v140 offset:24768
	ds_write_b32 v113, v141 offset:24772
	ds_write_b32 v113, v142 offset:24776
	ds_write_b32 v113, v143 offset:24780
	s_waitcnt vmcnt(3)
	ds_write_b32 v113, v144 offset:33024
	ds_write_b32 v113, v145 offset:33028
	ds_write_b32 v113, v146 offset:33032
	ds_write_b32 v113, v147 offset:33036
	s_waitcnt vmcnt(2)
	ds_write_b32 v113, v148 offset:41280
	ds_write_b32 v113, v149 offset:41284
	ds_write_b32 v113, v150 offset:41288
	ds_write_b32 v113, v151 offset:41292
	s_waitcnt vmcnt(1)
	ds_write_b32 v113, v152 offset:49536
	ds_write_b32 v113, v153 offset:49540
	ds_write_b32 v113, v154 offset:49544
	ds_write_b32 v113, v155 offset:49548
	s_waitcnt vmcnt(0)
	ds_write_b32 v113, v156 offset:57792
	ds_write_b32 v113, v157 offset:57796
	ds_write_b32 v113, v158 offset:57800
	ds_write_b32 v113, v159 offset:57804
	s_waitcnt lgkmcnt(0)
	s_barrier
	ds_read_b32 v160, v114
	ds_read_b32 v161, v114 offset:516
	ds_read_b32 v162, v114 offset:1032
	ds_read_b32 v163, v114 offset:1548
	ds_read_b32 v164, v114 offset:2064
	ds_read_b32 v165, v114 offset:2580
	ds_read_b32 v166, v114 offset:3096
	ds_read_b32 v167, v114 offset:3612
	s_waitcnt lgkmcnt(0)
	v_cvt_pk_bf16_f32 v168, v160, v161
	v_cvt_pk_bf16_f32 v169, v162, v163
	v_cvt_pk_bf16_f32 v170, v164, v165
	v_cvt_pk_bf16_f32 v171, v166, v167
	global_store_dwordx4 v115, v[168:171], s[28:29]
	ds_read_b32 v160, v114 offset:128
	ds_read_b32 v161, v114 offset:644
	ds_read_b32 v162, v114 offset:1160
	ds_read_b32 v163, v114 offset:1676
	ds_read_b32 v164, v114 offset:2192
	ds_read_b32 v165, v114 offset:2708
	ds_read_b32 v166, v114 offset:3224
	ds_read_b32 v167, v114 offset:3740
	s_waitcnt lgkmcnt(0)
	v_cvt_pk_bf16_f32 v172, v160, v161
	v_cvt_pk_bf16_f32 v173, v162, v163
	v_cvt_pk_bf16_f32 v174, v164, v165
	v_cvt_pk_bf16_f32 v175, v166, v167
	global_store_dwordx4 v116, v[172:175], s[28:29]
	ds_read_b32 v160, v114 offset:256
	ds_read_b32 v161, v114 offset:772
	ds_read_b32 v162, v114 offset:1288
	ds_read_b32 v163, v114 offset:1804
	ds_read_b32 v164, v114 offset:2320
	ds_read_b32 v165, v114 offset:2836
	ds_read_b32 v166, v114 offset:3352
	ds_read_b32 v167, v114 offset:3868
	s_waitcnt lgkmcnt(0)
	v_cvt_pk_bf16_f32 v168, v160, v161
	v_cvt_pk_bf16_f32 v169, v162, v163
	v_cvt_pk_bf16_f32 v170, v164, v165
	v_cvt_pk_bf16_f32 v171, v166, v167
	global_store_dwordx4 v117, v[168:171], s[28:29]
	ds_read_b32 v160, v114 offset:384
	ds_read_b32 v161, v114 offset:900
	ds_read_b32 v162, v114 offset:1416
	ds_read_b32 v163, v114 offset:1932
	ds_read_b32 v164, v114 offset:2448
	ds_read_b32 v165, v114 offset:2964
	ds_read_b32 v166, v114 offset:3480
	ds_read_b32 v167, v114 offset:3996
	s_waitcnt lgkmcnt(0)
	v_cvt_pk_bf16_f32 v172, v160, v161
	v_cvt_pk_bf16_f32 v173, v162, v163
	v_cvt_pk_bf16_f32 v174, v164, v165
	v_cvt_pk_bf16_f32 v175, v166, v167
	global_store_dwordx4 v118, v[172:175], s[28:29]
	v_cmp_eq_u32_e32 vcc, 0, v0
	s_and_saveexec_b64 s[34:35], vcc
	s_cbranch_execz .Lcvb_t0c
	s_waitcnt vmcnt(0)
	ds_write_b32 v125, v123
